# each wave starts layer 1 with its own two k-steps straight from the layer-0 registers (per-wave k rotation); h1 barrier moved behind them
# speedup vs baseline: 1.0157x; 1.0052x over previous
_Z16pdag_main_kernelPKfS0_S0_PKDv8_DF16_S3_S0_PKDF16_S5_S0_Pf:
	s_load_dwordx8 s[4:11], s[0:1], 0x0
	s_load_dwordx8 s[12:19], s[0:1], 0x20
	s_lshl_b32 s2, s2, 6
	s_ashr_i32 s3, s2, 31
	s_lshl_b64 s[24:25], s[2:3], 6
	v_mov_b32_e32 v136, 0
	s_waitcnt lgkmcnt(0)
	s_add_u32 s4, s4, s24
	s_addc_u32 s5, s5, s25
	v_lshlrev_b32_e32 v146, 2, v0
	v_lshlrev_b32_e32 v172, 4, v0
	v_mov_b32_e32 v173, v136
	global_load_dword v174, v146, s[4:5]
	global_load_dword v175, v146, s[4:5] offset:2048
	v_lshl_add_u64 v[2:3], s[14:15], 0, v[172:173]
	s_movk_i32 s4, 0x2000
	v_add_co_u32_e32 v4, vcc, s4, v2
	s_movk_i32 s5, 0x4000
	s_nop 0
	v_addc_co_u32_e32 v5, vcc, 0, v3, vcc
	v_add_co_u32_e32 v6, vcc, s5, v2
	s_movk_i32 s5, 0x6000
	s_nop 0
	v_addc_co_u32_e32 v7, vcc, 0, v3, vcc
	v_add_co_u32_e32 v2, vcc, s5, v2
	v_and_b32_e32 v1, 15, v0
	s_nop 0
	v_addc_co_u32_e32 v3, vcc, 0, v3, vcc
	global_load_dwordx4 v[148:151], v[4:5], off
	global_load_dwordx4 v[152:155], v[6:7], off
	global_load_dwordx4 v[156:159], v[2:3], off
	v_lshl_add_u64 v[2:3], s[16:17], 0, v[172:173]
	v_or_b32_e32 v10, s2, v1
	v_add_co_u32_e32 v2, vcc, s4, v2
	v_or_b32_e32 v12, 16, v10
	s_nop 0
	v_addc_co_u32_e32 v3, vcc, 0, v3, vcc
	v_ashrrev_i32_e32 v11, 31, v10
	v_mad_i64_i32 v[6:7], s[4:5], v10, 40, s[6:7]
	v_ashrrev_i32_e32 v13, 31, v12
	global_load_dwordx4 v[160:163], v172, s[14:15]
	global_load_dwordx4 v[164:167], v172, s[16:17]
	global_load_dwordx4 v[168:171], v[2:3], off
	global_load_dwordx2 v[144:145], v[6:7], off offset:32
	s_nop 0
	global_load_dwordx4 v[2:5], v[6:7], off offset:16
	global_load_dwordx4 v[126:129], v[6:7], off
	v_lshl_add_u64 v[6:7], v[10:11], 4, s[8:9]
	v_mad_i64_i32 v[14:15], s[4:5], v12, 40, s[6:7]
	v_lshl_add_u64 v[12:13], v[12:13], 4, s[8:9]
	global_load_dwordx4 v[122:125], v[6:7], off
	global_load_dwordx2 v[142:143], v[14:15], off offset:32
	s_nop 0
	global_load_dwordx4 v[6:9], v[14:15], off offset:16
	global_load_dwordx4 v[118:121], v[14:15], off
	global_load_dwordx4 v[114:117], v[12:13], off
	v_or_b32_e32 v12, 32, v10
	v_ashrrev_i32_e32 v13, 31, v12
	v_readfirstlane_b32 s22, v0
	v_mad_i64_i32 v[18:19], s[4:5], v12, 40, s[6:7]
	v_lshl_add_u64 v[12:13], v[12:13], 4, s[8:9]
	v_or_b32_e32 v10, 48, v10
	s_mov_b32 s21, 0
	s_lshr_b32 s20, s22, 6
	global_load_dwordx2 v[140:141], v[18:19], off offset:32
	global_load_dwordx4 v[14:17], v[18:19], off offset:16
	global_load_dwordx4 v[110:113], v[18:19], off
	global_load_dwordx4 v[106:109], v[12:13], off
	v_ashrrev_i32_e32 v11, 31, v10
	v_mad_i64_i32 v[12:13], s[4:5], v10, 40, s[6:7]
	v_lshl_add_u64 v[10:11], v[10:11], 4, s[8:9]
	s_lshl_b64 s[4:5], s[20:21], 16
	global_load_dwordx2 v[138:139], v[12:13], off offset:32
	global_load_dwordx4 v[26:29], v[12:13], off offset:16
	global_load_dwordx4 v[102:105], v[12:13], off
	global_load_dwordx4 v[98:101], v[10:11], off
	s_add_u32 s4, s12, s4
	v_and_b32_e32 v10, 31, v0
	s_addc_u32 s5, s13, s5
	v_lshlrev_b32_e32 v130, 4, v10
	s_lshl_b64 s[6:7], s[20:21], 7
	global_load_dwordx4 v[30:33], v130, s[4:5]
	global_load_dwordx4 v[22:25], v130, s[4:5] offset:1024
	global_load_dwordx4 v[18:21], v130, s[4:5] offset:2048
	global_load_dwordx4 v[10:13], v130, s[4:5] offset:3072
	s_add_u32 s8, s18, s6
	s_addc_u32 s9, s19, s7
	v_lshlrev_b32_e32 v132, 3, v1
	global_load_dwordx2 v[134:135], v132, s[8:9]
	s_load_dwordx4 s[12:15], s[0:1], 0x40
	v_and_b32_e32 v137, 63, v0
	v_mov_b32_e32 v131, v136
	v_mov_b32_e32 v133, v136
	v_lshlrev_b32_e32 v34, 4, v137
	s_mov_b32 s19, 0x20000
	s_mov_b32 s18, 0x880000
	s_and_b32 s17, s11, 0xffff
	s_mov_b32 s16, s10
	v_lshl_or_b32 v147, s20, 12, v34
	s_lshl_b32 s55, s20, 1
	s_add_i32 s56, s55, 0
	s_and_b32 s56, s56, 15
	s_lshl_b32 s60, s56, 15
	s_add_i32 s56, s55, 1
	s_and_b32 s56, s56, 15
	s_lshl_b32 s61, s56, 15
	s_add_i32 s56, s55, 2
	s_and_b32 s56, s56, 15
	s_lshl_b32 s62, s56, 15
	s_add_i32 s56, s55, 3
	s_and_b32 s56, s56, 15
	s_lshl_b32 s63, s56, 15
	s_add_i32 s56, s55, 4
	s_and_b32 s56, s56, 15
	s_lshl_b32 s56, s56, 15
	s_add_i32 s34, s56, 0xfff68000
	s_add_i32 s56, s55, 5
	s_and_b32 s56, s56, 15
	s_lshl_b32 s56, s56, 15
	s_add_i32 s35, s56, 0xfff68000
	s_add_i32 s56, s55, 6
	s_and_b32 s56, s56, 15
	s_lshl_b32 s56, s56, 15
	s_add_i32 s36, s56, 0xfff68000
	s_add_i32 s56, s55, 7
	s_and_b32 s56, s56, 15
	s_lshl_b32 s56, s56, 15
	s_add_i32 s37, s56, 0xfff68000
	s_add_i32 s56, s55, 8
	s_and_b32 s56, s56, 15
	s_lshl_b32 s56, s56, 15
	s_add_i32 s38, s56, 0xfff68000
	s_add_i32 s56, s55, 9
	s_and_b32 s56, s56, 15
	s_lshl_b32 s56, s56, 15
	s_add_i32 s39, s56, 0xfff68000
	s_add_i32 s56, s55, 10
	s_and_b32 s56, s56, 15
	s_lshl_b32 s56, s56, 15
	s_add_i32 s40, s56, 0xfff68000
	s_add_i32 s56, s55, 11
	s_and_b32 s56, s56, 15
	s_lshl_b32 s56, s56, 15
	s_add_i32 s41, s56, 0xfff68000
	s_add_i32 s56, s55, 12
	s_and_b32 s56, s56, 15
	s_lshl_b32 s56, s56, 15
	s_add_i32 s42, s56, 0xfff68000
	s_add_i32 s56, s55, 13
	s_and_b32 s56, s56, 15
	s_lshl_b32 s56, s56, 15
	s_add_i32 s43, s56, 0xfff68000
	s_add_i32 s56, s55, 14
	s_and_b32 s56, s56, 15
	s_lshl_b32 s56, s56, 15
	s_add_i32 s44, s56, 0xfff68000
	s_add_i32 s56, s55, 15
	s_and_b32 s56, s56, 15
	s_lshl_b32 s56, s56, 15
	s_add_i32 s45, s56, 0xfff68000
	s_add_i32 s56, s55, 16
	s_and_b32 s56, s56, 15
	s_lshl_b32 s56, s56, 15
	s_add_i32 s46, s56, 0xfffe8000
	s_add_i32 s56, s55, 17
	s_and_b32 s56, s56, 15
	s_lshl_b32 s56, s56, 15
	s_add_i32 s47, s56, 0xfffe8000
	s_add_i32 s56, s55, 18
	s_and_b32 s56, s56, 15
	s_lshl_b32 s56, s56, 15
	s_add_i32 s48, s56, 0xfffe8000
	s_add_i32 s56, s55, 19
	s_and_b32 s56, s56, 15
	s_lshl_b32 s56, s56, 15
	s_add_i32 s49, s56, 0xfffe8000
	s_add_i32 s56, s55, 0
	s_and_b32 s56, s56, 15
	s_lshr_b32 s56, s56, 2
	s_add_i32 s57, s55, 12
	s_and_b32 s57, s57, 15
	s_lshr_b32 s57, s57, 2
	s_sub_i32 s56, s56, s57
	s_lshl_b32 s64, s56, 8
	s_add_i32 s56, s55, 1
	s_and_b32 s56, s56, 15
	s_lshr_b32 s56, s56, 2
	s_add_i32 s57, s55, 13
	s_and_b32 s57, s57, 15
	s_lshr_b32 s57, s57, 2
	s_sub_i32 s56, s56, s57
	s_lshl_b32 s65, s56, 8
	s_add_i32 s56, s55, 2
	s_and_b32 s56, s56, 15
	s_lshr_b32 s56, s56, 2
	s_add_i32 s57, s55, 14
	s_and_b32 s57, s57, 15
	s_lshr_b32 s57, s57, 2
	s_sub_i32 s56, s56, s57
	s_lshl_b32 s66, s56, 8
	s_add_i32 s56, s55, 3
	s_and_b32 s56, s56, 15
	s_lshr_b32 s56, s56, 2
	s_add_i32 s57, s55, 15
	s_and_b32 s57, s57, 15
	s_lshr_b32 s57, s57, 2
	s_sub_i32 s56, s56, s57
	s_lshl_b32 s67, s56, 8
	s_add_i32 s56, s55, 4
	s_and_b32 s56, s56, 15
	s_lshr_b32 s56, s56, 2
	s_add_i32 s57, s55, 16
	s_and_b32 s57, s57, 15
	s_lshr_b32 s57, s57, 2
	s_sub_i32 s56, s56, s57
	s_lshl_b32 s68, s56, 8
	s_add_i32 s56, s55, 5
	s_and_b32 s56, s56, 15
	s_lshr_b32 s56, s56, 2
	s_add_i32 s57, s55, 17
	s_and_b32 s57, s57, 15
	s_lshr_b32 s57, s57, 2
	s_sub_i32 s56, s56, s57
	s_lshl_b32 s69, s56, 8
	s_add_i32 s56, s55, 6
	s_and_b32 s56, s56, 15
	s_lshr_b32 s56, s56, 2
	s_add_i32 s57, s55, 18
	s_and_b32 s57, s57, 15
	s_lshr_b32 s57, s57, 2
	s_sub_i32 s56, s56, s57
	s_lshl_b32 s70, s56, 8
	s_add_i32 s56, s55, 7
	s_and_b32 s56, s56, 15
	s_lshr_b32 s56, s56, 2
	s_add_i32 s57, s55, 19
	s_and_b32 s57, s57, 15
	s_lshr_b32 s57, s57, 2
	s_sub_i32 s56, s56, s57
	s_lshl_b32 s71, s56, 8
	s_add_i32 s56, s55, 8
	s_and_b32 s56, s56, 15
	s_lshr_b32 s56, s56, 2
	s_add_i32 s57, s55, 20
	s_and_b32 s57, s57, 15
	s_lshr_b32 s57, s57, 2
	s_sub_i32 s56, s56, s57
	s_lshl_b32 s72, s56, 8
	s_add_i32 s56, s55, 9
	s_and_b32 s56, s56, 15
	s_lshr_b32 s56, s56, 2
	s_add_i32 s57, s55, 21
	s_and_b32 s57, s57, 15
	s_lshr_b32 s57, s57, 2
	s_sub_i32 s56, s56, s57
	s_lshl_b32 s73, s56, 8
	s_add_i32 s56, s55, 10
	s_and_b32 s56, s56, 15
	s_lshr_b32 s56, s56, 2
	s_add_i32 s57, s55, 22
	s_and_b32 s57, s57, 15
	s_lshr_b32 s57, s57, 2
	s_sub_i32 s56, s56, s57
	s_lshl_b32 s74, s56, 8
	s_add_i32 s56, s55, 11
	s_and_b32 s56, s56, 15
	s_lshr_b32 s56, s56, 2
	s_add_i32 s57, s55, 23
	s_and_b32 s57, s57, 15
	s_lshr_b32 s57, s57, 2
	s_sub_i32 s56, s56, s57
	s_lshl_b32 s75, s56, 8
	s_add_i32 s56, s55, 12
	s_and_b32 s56, s56, 15
	s_lshr_b32 s56, s56, 2
	s_add_i32 s57, s55, 24
	s_and_b32 s57, s57, 15
	s_lshr_b32 s57, s57, 2
	s_sub_i32 s56, s56, s57
	s_lshl_b32 s76, s56, 8
	s_add_i32 s56, s55, 13
	s_and_b32 s56, s56, 15
	s_lshr_b32 s56, s56, 2
	s_add_i32 s57, s55, 25
	s_and_b32 s57, s57, 15
	s_lshr_b32 s57, s57, 2
	s_sub_i32 s56, s56, s57
	s_lshl_b32 s77, s56, 8
	s_add_i32 s56, s55, 14
	s_and_b32 s56, s56, 15
	s_lshr_b32 s56, s56, 2
	s_add_i32 s57, s55, 26
	s_and_b32 s57, s57, 15
	s_lshr_b32 s57, s57, 2
	s_sub_i32 s56, s56, s57
	s_lshl_b32 s78, s56, 8
	s_add_i32 s56, s55, 15
	s_and_b32 s56, s56, 15
	s_lshr_b32 s56, s56, 2
	s_add_i32 s57, s55, 27
	s_and_b32 s57, s57, 15
	s_lshr_b32 s57, s57, 2
	s_sub_i32 s56, s56, s57
	s_lshl_b32 s79, s56, 8
	s_add_i32 s56, s55, 12
	s_and_b32 s56, s56, 15
	s_lshr_b32 s56, s56, 2
	s_lshl_b32 s80, s56, 8
	s_add_i32 s56, s55, 13
	s_and_b32 s56, s56, 15
	s_lshr_b32 s56, s56, 2
	s_lshl_b32 s81, s56, 8
	s_add_i32 s56, s55, 14
	s_and_b32 s56, s56, 15
	s_lshr_b32 s56, s56, 2
	s_lshl_b32 s82, s56, 8
	s_add_i32 s56, s55, 15
	s_and_b32 s56, s56, 15
	s_lshr_b32 s56, s56, 2
	s_lshl_b32 s83, s56, 8
	s_and_b32 s56, s20, 1
	s_cmp_eq_u32 s56, 1
	s_cselect_b64 s[84:85], -1, 0
	buffer_load_dwordx4 v[58:61], v147, s[16:19], s60 offen
	buffer_load_dwordx4 v[54:57], v147, s[16:19], s60 offen offset:1024
	buffer_load_dwordx4 v[50:53], v147, s[16:19], s60 offen offset:2048
	buffer_load_dwordx4 v[38:41], v147, s[16:19], s60 offen offset:3072
	s_mov_b32 s10, 0xffff
	s_mov_b32 s0, 0x8000
	buffer_load_dwordx4 v[94:97], v147, s[16:19], s61 offen
	buffer_load_dwordx4 v[90:93], v147, s[16:19], s61 offen offset:1024
	buffer_load_dwordx4 v[78:81], v147, s[16:19], s61 offen offset:2048
	buffer_load_dwordx4 v[34:37], v147, s[16:19], s61 offen offset:3072
	s_mov_b32 s0, 0x10000
	buffer_load_dwordx4 v[82:85], v147, s[16:19], s62 offen
	buffer_load_dwordx4 v[70:73], v147, s[16:19], s62 offen offset:1024
	buffer_load_dwordx4 v[62:65], v147, s[16:19], s62 offen offset:2048
	buffer_load_dwordx4 v[42:45], v147, s[16:19], s62 offen offset:3072
	s_mov_b32 s0, 0x18000
	buffer_load_dwordx4 v[86:89], v147, s[16:19], s63 offen
	buffer_load_dwordx4 v[74:77], v147, s[16:19], s63 offen offset:1024
	buffer_load_dwordx4 v[66:69], v147, s[16:19], s63 offen offset:2048
	buffer_load_dwordx4 v[46:49], v147, s[16:19], s63 offen offset:3072
	s_waitcnt vmcnt(44)
	v_cvt_f16_f32_e32 v173, v174
	s_waitcnt vmcnt(43)
	v_cvt_f16_f32_e32 v175, v175
	v_lshlrev_b32_e32 v174, 1, v0
	v_or_b32_e32 v176, 0x12400, v174
	ds_write_b16 v176, v173
	v_or_b32_e32 v173, 0x12800, v174
	ds_write_b16 v173, v175
	v_add_u32_e32 v173, 0x12c00, v172
	s_mov_b32 s11, 1
	s_waitcnt vmcnt(39)
	ds_write_b128 v173, v[160:163]
	ds_write_b128 v173, v[148:151] offset:8192
	ds_write_b128 v173, v[152:155] offset:16384
	ds_write_b128 v173, v[156:159] offset:24576
	v_add_u32_e32 v148, 0x1ac00, v172
	s_cmpk_lt_u32 s22, 0x100
	s_waitcnt vmcnt(38)
	ds_write_b128 v148, v[164:167]
	s_waitcnt vmcnt(37)
	ds_write_b128 v148, v[168:171] offset:8192
	s_cbranch_scc1 .LBB1_2
	s_setprio 3
.LBB1_2:
	v_lshrrev_b32_e32 v151, 4, v137
	s_lshl_b64 s[6:7], s[2:3], 4
	v_cmp_eq_u32_e64 s[2:3], 1, v151
	s_waitcnt vmcnt(31)
	v_cvt_f16_f32_e32 v8, v8
	v_cmp_gt_u32_e32 vcc, 16, v137
	s_waitcnt vmcnt(29)
	v_cndmask_b32_e64 v116, 0, v116, s[2:3]
	s_waitcnt vmcnt(21)
	v_cndmask_b32_e64 v100, 0, v100, s[2:3]
	v_cmp_eq_u32_e64 s[0:1], 2, v151
	v_cndmask_b32_e64 v114, 0, v114, s[2:3]
	v_cndmask_b32_e64 v115, 0, v115, s[2:3]
	v_cndmask_b32_e32 v6, v116, v6, vcc
	v_cndmask_b32_e64 v116, 0, v117, s[2:3]
	v_cndmask_b32_e64 v108, 0, v108, s[2:3]
	v_cndmask_b32_e32 v26, v100, v26, vcc
	v_cvt_f16_f32_e32 v29, v29
	v_cndmask_b32_e64 v100, 0, v101, s[2:3]
	v_cndmask_b32_e32 v28, 0, v28, vcc
	v_cndmask_b32_e64 v152, 0, 1.0, s[0:1]
	v_cndmask_b32_e32 v114, v114, v120, vcc
	v_cndmask_b32_e32 v115, v115, v121, vcc
	v_cndmask_b32_e32 v7, v116, v7, vcc
	v_cndmask_b32_e64 v106, 0, v106, s[2:3]
	v_cndmask_b32_e64 v107, 0, v107, s[2:3]
	v_cndmask_b32_e32 v14, v108, v14, vcc
	v_cndmask_b32_e64 v108, 0, v109, s[2:3]
	v_cndmask_b32_e32 v27, v100, v27, vcc
	v_cvt_f16_f32_e32 v100, v28
	v_cndmask_b32_e32 v116, 0, v8, vcc
	v_cvt_pk_f16_f32 v8, v6, v7
	v_cvt_pk_f16_f32 v7, v114, v115
	v_cndmask_b32_e64 v114, v152, v140, s[2:3]
	v_cndmask_b32_e32 v106, v106, v112, vcc
	v_cndmask_b32_e32 v107, v107, v113, vcc
	v_cndmask_b32_e32 v15, v108, v15, vcc
	v_cndmask_b32_e64 v98, 0, v98, s[2:3]
	v_cndmask_b32_e64 v99, 0, v99, s[2:3]
	v_cndmask_b32_e32 v110, v114, v110, vcc
	v_cndmask_b32_e64 v114, 0, v141, s[2:3]
	v_cndmask_b32_e32 v108, 0, v16, vcc
	v_cvt_pk_f16_f32 v16, v14, v15
	v_cvt_pk_f16_f32 v15, v106, v107
	v_cndmask_b32_e64 v106, v152, v138, s[2:3]
	v_cndmask_b32_e32 v98, v98, v104, vcc
	v_cndmask_b32_e32 v99, v99, v105, vcc
	v_cndmask_b32_e32 v111, v114, v111, vcc
	v_cndmask_b32_e32 v102, v106, v102, vcc
	v_cndmask_b32_e64 v106, 0, v139, s[2:3]
	v_cndmask_b32_e32 v29, 0, v29, vcc
	v_cvt_pk_f16_f32 v28, v26, v27
	v_cvt_pk_f16_f32 v27, v98, v99
	v_lshlrev_b32_e32 v101, 10, v1
	v_bitop3_b32 v98, v151, v0, 3 bitop3:0x78
	v_lshl_add_u64 v[130:131], s[4:5], 0, v[130:131]
	v_cvt_f16_f32_e32 v4, v4
	v_cvt_pk_f16_f32 v14, v110, v111
	v_cndmask_b32_e32 v103, v106, v103, vcc
	v_pack_b32_f16 v29, v100, v29
	v_lshl_or_b32 v111, v98, 4, v101
	v_lshlrev_b32_e32 v100, 4, v1
	s_movk_i32 s4, 0xc0
	v_cndmask_b32_e64 v124, 0, v124, s[2:3]
	v_cvt_pk_f16_f32 v26, v102, v103
	v_and_b32_e32 v112, 0xc0, v100
	v_bitop3_b32 v100, v100, s4, v111 bitop3:0x26
	s_lshl_b32 s4, s20, 3
	v_lshrrev_b32_e32 v102, 5, v137
	v_lshrrev_b32_e32 v104, 1, v137
	v_cndmask_b32_e64 v122, 0, v122, s[2:3]
	v_cndmask_b32_e64 v123, 0, v123, s[2:3]
	v_cndmask_b32_e32 v2, v124, v2, vcc
	v_cvt_f16_f32_e32 v5, v5
	v_cndmask_b32_e64 v124, 0, v125, s[2:3]
	v_cvt_f16_f32_e32 v9, v9
	v_or_b32_e32 v103, s4, v102
	v_and_or_b32 v110, v104, 8, v101
	v_bitop3_b32 v101, s4, v1, v102 bitop3:0x36
	s_lshl_b32 s4, s20, 4
	v_cndmask_b32_e32 v122, v122, v128, vcc
	v_cndmask_b32_e32 v123, v123, v129, vcc
	v_cndmask_b32_e32 v3, v124, v3, vcc
	v_cndmask_b32_e32 v17, 0, v17, vcc
	v_lshlrev_b32_e32 v107, 4, v101
	v_bitop3_b32 v101, v103, v1, 2 bitop3:0x36
	s_add_i32 s4, s4, 0x10000
	v_bfe_u32 v0, v0, 4, 2
	v_cndmask_b32_e64 v144, v152, v144, s[2:3]
	v_cndmask_b32_e32 v124, 0, v4, vcc
	v_cvt_pk_f16_f32 v4, v2, v3
	v_cvt_pk_f16_f32 v3, v122, v123
	v_cndmask_b32_e64 v122, v152, v142, s[2:3]
	v_cvt_pk_f16_f32 v17, v108, v17
	s_movk_i32 s5, 0x80
	v_lshlrev_b32_e32 v108, 4, v101
	v_bitop3_b32 v101, v103, v1, 4 bitop3:0x36
	s_cmp_lt_u32 s22, 64
	v_lshlrev_b32_e32 v104, 5, v0
	v_lshlrev_b32_e32 v0, 6, v0
	v_cndmask_b32_e32 v126, v144, v126, vcc
	v_cndmask_b32_e64 v144, 0, v145, s[2:3]
	v_cndmask_b32_e32 v118, v122, v118, vcc
	v_cndmask_b32_e64 v122, 0, v143, s[2:3]
	v_bitop3_b32 v99, v112, s5, v111 bitop3:0x36
	v_lshlrev_b32_e32 v109, 4, v101
	v_bitop3_b32 v101, v103, v1, 6 bitop3:0x36
	v_lshl_or_b32 v105, s20, 8, v0
	v_mov_b32_e32 v0, 0x1ec00
	s_cselect_b64 s[4:5], -1, 0
	v_cndmask_b32_e32 v127, v144, v127, vcc
	v_cndmask_b32_e32 v5, 0, v5, vcc
	v_cndmask_b32_e32 v119, v122, v119, vcc
	v_cndmask_b32_e32 v9, 0, v9, vcc
	v_lshlrev_b32_e32 v113, 4, v101
	v_lshlrev_b32_e32 v101, 5, v1
	v_lshl_add_u32 v106, v137, 6, v0
	s_cmp_eq_u32 s20, 0
	s_cselect_b32 s31, 0, 0xffff1d00
	v_add_u32_e32 v106, s31, v106
	v_cndmask_b32_e64 v0, 0, 1, s[4:5]
	v_lshl_add_u64 v[132:133], s[8:9], 0, v[132:133]
	v_or_b32_e32 v148, 0x400, v147
	v_or_b32_e32 v149, 0x800, v147
	v_or_b32_e32 v150, 0xc00, v147
	v_cvt_pk_f16_f32 v2, v126, v127
	v_pack_b32_f16 v5, v124, v5
	v_cvt_pk_f16_f32 v6, v118, v119
	v_pack_b32_f16 v9, v116, v9
	v_bitop3_b32 v98, v112, 64, v111 bitop3:0x36
	v_lshl_or_b32 v104, s20, 7, v104
	s_mov_b32 s22, 0x98000
	s_mov_b32 s23, 0x5040100
	s_mov_b32 s24, 0x7060302
	v_add_u32_e32 v107, v107, v110
	v_add_u32_e32 v108, v108, v110
	v_add_u32_e32 v109, v109, v110
	v_add_u32_e32 v110, v113, v110
	v_add_u32_e32 v111, v112, v111
	v_lshlrev_b32_e32 v113, 4, v137
	v_or_b32_e32 v113, 0x10000, v113
	s_lshr_b32 s28, s20, 2
	s_and_b32 s29, s20, 3
	s_lshl_b32 s28, s28, 10
	s_lshl_b32 s29, s29, 2
	s_add_i32 s28, s28, s29
	v_add_u32_e32 v112, s28, v113
	v_cmp_eq_u32_e64 s[26:27], 3, v151
	v_add_u32_e32 v114, 0x12400, v101
	v_mov_b32_e32 v121, v111
	v_mov_b32_e32 v144, v98
	v_cndmask_b32_e64 v111, v111, v99, s[84:85]
	v_cndmask_b32_e64 v99, v99, v121, s[84:85]
	v_cndmask_b32_e64 v98, v98, v100, s[84:85]
	v_cndmask_b32_e64 v100, v100, v144, s[84:85]
	v_add_u32_e32 v111, s80, v111
	v_add_u32_e32 v98, s81, v98
	v_add_u32_e32 v99, s82, v99
	v_add_u32_e32 v100, s83, v100
	v_and_b32_e32 v108, 15, v137
	s_lshl_b32 s31, s20, 3
	v_add_u32_e32 v107, s31, v151
	v_xor_b32_e32 v107, v107, v108
	v_lshlrev_b32_e32 v107, 4, v107
	v_lshl_or_b32 v107, v108, 10, v107
	v_xor_b32_e32 v108, 64, v107
	v_cmp_ne_u32_e64 s[4:5], 1, v0
	s_waitcnt vmcnt(16)
	v_cndmask_b32_e64 v1, v30, v134, s[0:1]
	v_bfi_b32 v30, s10, v1, v30
	v_perm_b32 v1, v22, v134, s24
	v_cndmask_b32_e64 v22, v22, v1, s[0:1]
	v_bfi_b32 v1, s10, v135, v18
	v_perm_b32 v121, v10, v135, s24
	v_cndmask_b32_e64 v18, v18, v1, s[0:1]
	v_cndmask_b32_e64 v10, v10, v121, s[0:1]
	v_mov_b32_e32 v121, v136
	v_mov_b32_e32 v144, v136
	v_mov_b32_e32 v145, v136
	v_mov_b32_e32 v0, v136
	v_mov_b32_e32 v1, v136
	s_waitcnt lgkmcnt(0)
	s_barrier
	ds_read_u16 v102, v114
	ds_read_u16 v103, v114 offset:512
	ds_read_u16 v115, v114 offset:1024
	ds_read_u16 v116, v114 offset:1536
	v_add_u32_e32 v0, 0x12c00, v105
	ds_read_b128 v[240:243], v0
	ds_read_b128 v[244:247], v0 offset:16
	ds_read_b128 v[248:251], v0 offset:32
	ds_read_b128 v[252:255], v0 offset:48
	v_add_u32_e32 v114, 2, v114
	s_waitcnt lgkmcnt(0)
	s_branch .LBB1_4
.LBB1_4:
	s_and_saveexec_b64 s[8:9], s[2:3]
	v_perm_b32 v5, v1, v102, s23
	v_perm_b32 v9, v121, v103, s23
	v_perm_b32 v17, v144, v115, s23
	v_perm_b32 v29, v145, v116, s23
	s_or_b64 exec, exec, s[8:9]
	v_mfma_f32_16x16x32_f16 v[164:167], v[30:33], v[2:5], 0
	v_mfma_f32_16x16x32_f16 v[180:183], v[22:25], v[2:5], 0
	s_cmp_lg_u32 s22, 0x818000
	v_mfma_f32_16x16x32_f16 v[168:171], v[30:33], v[6:9], 0
	v_mfma_f32_16x16x32_f16 v[184:187], v[22:25], v[6:9], 0
	s_cselect_b32 s9, s11, 15
	v_mfma_f32_16x16x32_f16 v[172:175], v[30:33], v[14:17], 0
	v_mfma_f32_16x16x32_f16 v[188:191], v[22:25], v[14:17], 0
	v_mfma_f32_16x16x32_f16 v[176:179], v[30:33], v[26:29], 0
	v_mfma_f32_16x16x32_f16 v[192:195], v[22:25], v[26:29], 0
	v_mfma_f32_16x16x32_f16 v[196:199], v[18:21], v[2:5], 0
	v_cvt_pk_f16_f32 v122, v164, v165
	v_cvt_pk_f16_f32 v123, v166, v167
	v_pk_max_f16 v122, v122, 0
	v_pk_max_f16 v123, v123, 0
	v_cvt_pk_f16_f32 v124, v180, v181
	v_cvt_pk_f16_f32 v125, v182, v183
	v_pk_max_f16 v124, v124, 0
	v_pk_max_f16 v125, v125, 0
	ds_write_b128 v107, v[122:125]
	v_mfma_f32_16x16x32_f16 v[212:215], v[10:13], v[2:5], 0
	v_cvt_pk_f16_f32 v126, v168, v169
	v_cvt_pk_f16_f32 v127, v170, v171
	v_pk_max_f16 v126, v126, 0
	v_pk_max_f16 v127, v127, 0
	v_cvt_pk_f16_f32 v128, v184, v185
	v_cvt_pk_f16_f32 v129, v186, v187
	v_pk_max_f16 v128, v128, 0
	v_pk_max_f16 v129, v129, 0
	ds_write_b128 v107, v[126:129] offset:16384
	v_mfma_f32_16x16x32_f16 v[200:203], v[18:21], v[6:9], 0
	v_cvt_pk_f16_f32 v134, v172, v173
	v_cvt_pk_f16_f32 v135, v174, v175
	v_pk_max_f16 v134, v134, 0
	v_pk_max_f16 v135, v135, 0
	v_cvt_pk_f16_f32 v136, v188, v189
	v_cvt_pk_f16_f32 v137, v190, v191
	v_pk_max_f16 v136, v136, 0
	v_pk_max_f16 v137, v137, 0
	ds_write_b128 v107, v[134:137] offset:32768
	v_mfma_f32_16x16x32_f16 v[216:219], v[10:13], v[6:9], 0
	v_cvt_pk_f16_f32 v138, v176, v177
	v_cvt_pk_f16_f32 v139, v178, v179
	v_pk_max_f16 v138, v138, 0
	v_pk_max_f16 v139, v139, 0
	v_cvt_pk_f16_f32 v140, v192, v193
	v_cvt_pk_f16_f32 v141, v194, v195
	v_pk_max_f16 v140, v140, 0
	v_pk_max_f16 v141, v141, 0
	ds_write_b128 v107, v[138:141] offset:49152
	v_mfma_f32_16x16x32_f16 v[204:207], v[18:21], v[14:17], 0
	v_cvt_pk_f16_f32 v142, v196, v197
	v_cvt_pk_f16_f32 v143, v198, v199
	v_pk_max_f16 v142, v142, 0
	v_pk_max_f16 v143, v143, 0
	v_cvt_pk_f16_f32 v144, v212, v213
	v_cvt_pk_f16_f32 v145, v214, v215
	v_pk_max_f16 v144, v144, 0
	v_pk_max_f16 v145, v145, 0
	ds_write_b128 v108, v[142:145]
	v_mfma_f32_16x16x32_f16 v[220:223], v[10:13], v[14:17], 0
	v_cvt_pk_f16_f32 v152, v200, v201
	v_cvt_pk_f16_f32 v153, v202, v203
	v_pk_max_f16 v152, v152, 0
	v_pk_max_f16 v153, v153, 0
	v_cvt_pk_f16_f32 v154, v216, v217
	v_cvt_pk_f16_f32 v155, v218, v219
	v_pk_max_f16 v154, v154, 0
	v_pk_max_f16 v155, v155, 0
	ds_write_b128 v108, v[152:155] offset:16384
	v_mfma_f32_16x16x32_f16 v[208:211], v[18:21], v[26:29], 0
	v_mfma_f32_16x16x32_f16 v[224:227], v[10:13], v[26:29], 0
	v_cvt_pk_f16_f32 v156, v204, v205
	v_cvt_pk_f16_f32 v157, v206, v207
	v_pk_max_f16 v156, v156, 0
	v_pk_max_f16 v157, v157, 0
	v_cvt_pk_f16_f32 v158, v220, v221
	v_cvt_pk_f16_f32 v159, v222, v223
	v_pk_max_f16 v158, v158, 0
	v_pk_max_f16 v159, v159, 0
	ds_write_b128 v108, v[156:159] offset:32768
	v_cvt_pk_f16_f32 v160, v208, v209
	v_cvt_pk_f16_f32 v161, v210, v211
	v_pk_max_f16 v160, v160, 0
	v_pk_max_f16 v161, v161, 0
	v_cvt_pk_f16_f32 v162, v224, v225
	v_cvt_pk_f16_f32 v163, v226, v227
	v_pk_max_f16 v162, v162, 0
	v_pk_max_f16 v163, v163, 0
	ds_write_b128 v108, v[160:163] offset:49152
	v_add_u32_e32 v111, s64, v111
	v_add_u32_e32 v98, s65, v98
	s_lshl_b32 s20, s9, 7
	v_lshl_add_u64 v[0:1], s[20:21], 3, v[132:133]
	s_add_i32 s25, s22, s34
	s_lshl_b32 s8, s9, 8
	buffer_load_dwordx4 v[192:195], v147, s[16:19], s25 offen
	buffer_load_dwordx4 v[196:199], v148, s[16:19], s25 offen
	buffer_load_dwordx4 v[200:203], v149, s[16:19], s25 offen
	buffer_load_dwordx4 v[204:207], v150, s[16:19], s25 offen
	s_waitcnt vmcnt(19)
	v_mfma_f32_16x16x32_f16 v[164:167], v[58:61], v[122:125], v[240:243]
	v_mfma_f32_16x16x32_f16 v[168:171], v[58:61], v[126:129], v[240:243]
	v_mfma_f32_16x16x32_f16 v[172:175], v[58:61], v[134:137], v[240:243]
	v_mfma_f32_16x16x32_f16 v[10:13], v[58:61], v[138:141], v[240:243]
	s_waitcnt vmcnt(18)
	v_mfma_f32_16x16x32_f16 v[58:61], v[54:57], v[122:125], v[244:247]
	v_mfma_f32_16x16x32_f16 v[176:179], v[54:57], v[126:129], v[244:247]
	v_mfma_f32_16x16x32_f16 v[180:183], v[54:57], v[134:137], v[244:247]
	v_mfma_f32_16x16x32_f16 v[18:21], v[54:57], v[138:141], v[244:247]
	s_waitcnt vmcnt(17)
	v_mfma_f32_16x16x32_f16 v[54:57], v[50:53], v[122:125], v[248:251]
	v_mfma_f32_16x16x32_f16 v[184:187], v[50:53], v[126:129], v[248:251]
	v_mfma_f32_16x16x32_f16 v[188:191], v[50:53], v[134:137], v[248:251]
	v_mfma_f32_16x16x32_f16 v[22:25], v[50:53], v[138:141], v[248:251]
	s_waitcnt vmcnt(16)
	v_mfma_f32_16x16x32_f16 v[50:53], v[38:41], v[122:125], v[252:255]
	v_mfma_f32_16x16x32_f16 v[122:125], v[38:41], v[126:129], v[252:255]
	v_mfma_f32_16x16x32_f16 v[126:129], v[38:41], v[134:137], v[252:255]
	v_mfma_f32_16x16x32_f16 v[38:41], v[38:41], v[138:141], v[252:255]
	s_add_i32 s9, s22, s35
	s_waitcnt vmcnt(15)
	v_mfma_f32_16x16x32_f16 v[164:167], v[94:97], v[142:145], v[164:167]
	v_mfma_f32_16x16x32_f16 v[168:171], v[94:97], v[152:155], v[168:171]
	s_waitcnt vmcnt(14)
	v_mfma_f32_16x16x32_f16 v[58:61], v[90:93], v[142:145], v[58:61]
	v_mfma_f32_16x16x32_f16 v[176:179], v[90:93], v[152:155], v[176:179]
	s_waitcnt vmcnt(13)
	v_mfma_f32_16x16x32_f16 v[54:57], v[78:81], v[142:145], v[54:57]
	v_mfma_f32_16x16x32_f16 v[184:187], v[78:81], v[152:155], v[184:187]
	s_waitcnt vmcnt(12)
	v_mfma_f32_16x16x32_f16 v[50:53], v[34:37], v[142:145], v[50:53]
	buffer_load_dwordx4 v[140:143], v147, s[16:19], s9 offen
	buffer_load_dwordx4 v[220:223], v148, s[16:19], s9 offen
	v_mfma_f32_16x16x32_f16 v[122:125], v[34:37], v[152:155], v[122:125]
	buffer_load_dwordx4 v[152:155], v149, s[16:19], s9 offen
	buffer_load_dwordx4 v[224:227], v150, s[16:19], s9 offen
	s_mov_b32 s9, s21
	v_mfma_f32_16x16x32_f16 v[172:175], v[94:97], v[156:159], v[172:175]
	v_mfma_f32_16x16x32_f16 v[94:97], v[94:97], v[160:163], v[10:13]
	s_nop 2
	v_lshl_add_u64 v[10:11], s[8:9], 4, v[130:131]
	v_mfma_f32_16x16x32_f16 v[180:183], v[90:93], v[156:159], v[180:183]
	v_mfma_f32_16x16x32_f16 v[90:93], v[90:93], v[160:163], v[18:21]
	v_mfma_f32_16x16x32_f16 v[188:191], v[78:81], v[156:159], v[188:191]
	v_mfma_f32_16x16x32_f16 v[78:81], v[78:81], v[160:163], v[22:25]
	global_load_dwordx4 v[30:33], v[10:11], off
	s_nop 1
	global_load_dwordx4 v[22:25], v[10:11], off offset:1024
	global_load_dwordx4 v[18:21], v[10:11], off offset:2048
	s_nop 0
	global_load_dwordx4 v[10:13], v[10:11], off offset:3072
	s_nop 0
	global_load_dwordx2 v[134:135], v[0:1], off
	v_mfma_f32_16x16x32_f16 v[126:129], v[34:37], v[156:159], v[126:129]
	v_mfma_f32_16x16x32_f16 v[34:37], v[34:37], v[160:163], v[38:41]
	s_waitcnt lgkmcnt(0)
	s_barrier
	v_add_u32_e32 v99, s66, v99
	ds_read_b128 v[136:139], v99
	ds_read_b128 v[208:211], v99 offset:16384
	ds_read_b128 v[212:215], v99 offset:32768
	ds_read_b128 v[216:219], v99 offset:49152
	s_nop 2
	v_add_u32_e32 v100, s67, v100
	ds_read_b128 v[38:41], v100
	ds_read_b128 v[156:159], v100 offset:16384
	ds_read_b128 v[160:163], v100 offset:32768
	ds_read_b128 v[228:231], v100 offset:49152
	s_add_i32 s8, s22, s36
	s_waitcnt vmcnt(20) lgkmcnt(7)
	v_mfma_f32_16x16x32_f16 v[164:167], v[82:85], v[136:139], v[164:167]
	s_waitcnt lgkmcnt(6)
	v_mfma_f32_16x16x32_f16 v[168:171], v[82:85], v[208:211], v[168:171]
	s_waitcnt lgkmcnt(5)
	v_mfma_f32_16x16x32_f16 v[172:175], v[82:85], v[212:215], v[172:175]
	s_waitcnt lgkmcnt(4)
	v_mfma_f32_16x16x32_f16 v[82:85], v[82:85], v[216:219], v[94:97]
	s_waitcnt vmcnt(19)
	v_mfma_f32_16x16x32_f16 v[58:61], v[70:73], v[136:139], v[58:61]
	v_mfma_f32_16x16x32_f16 v[94:97], v[70:73], v[208:211], v[176:179]
	v_mfma_f32_16x16x32_f16 v[176:179], v[70:73], v[212:215], v[180:183]
	v_mfma_f32_16x16x32_f16 v[70:73], v[70:73], v[216:219], v[90:93]
	s_waitcnt vmcnt(18)
	v_mfma_f32_16x16x32_f16 v[54:57], v[62:65], v[136:139], v[54:57]
	v_mfma_f32_16x16x32_f16 v[90:93], v[62:65], v[208:211], v[184:187]
	v_mfma_f32_16x16x32_f16 v[180:183], v[62:65], v[212:215], v[188:191]
	v_mfma_f32_16x16x32_f16 v[62:65], v[62:65], v[216:219], v[78:81]
	s_waitcnt vmcnt(17)
	v_mfma_f32_16x16x32_f16 v[50:53], v[42:45], v[136:139], v[50:53]
	v_mfma_f32_16x16x32_f16 v[78:81], v[42:45], v[208:211], v[122:125]
	v_mfma_f32_16x16x32_f16 v[122:125], v[42:45], v[212:215], v[126:129]
	s_nop 2
	buffer_load_dwordx4 v[126:129], v147, s[16:19], s8 offen
	buffer_load_dwordx4 v[136:139], v148, s[16:19], s8 offen
	buffer_load_dwordx4 v[184:187], v149, s[16:19], s8 offen
	buffer_load_dwordx4 v[188:191], v150, s[16:19], s8 offen
	v_mfma_f32_16x16x32_f16 v[34:37], v[42:45], v[216:219], v[34:37]
	v_add_u32_e32 v111, s68, v111
	ds_read_b128 v[42:45], v111
	ds_read_b128 v[208:211], v111 offset:16384
	ds_read_b128 v[212:215], v111 offset:32768
	ds_read_b128 v[216:219], v111 offset:49152
	s_add_i32 s8, s22, s37
	s_waitcnt vmcnt(20) lgkmcnt(7)
	v_mfma_f32_16x16x32_f16 v[164:167], v[86:89], v[38:41], v[164:167]
	s_waitcnt lgkmcnt(6)
	v_mfma_f32_16x16x32_f16 v[168:171], v[86:89], v[156:159], v[168:171]
	s_waitcnt lgkmcnt(5)
	v_mfma_f32_16x16x32_f16 v[172:175], v[86:89], v[160:163], v[172:175]
	s_waitcnt lgkmcnt(4)
	v_mfma_f32_16x16x32_f16 v[82:85], v[86:89], v[228:231], v[82:85]
	s_waitcnt vmcnt(19)
	v_mfma_f32_16x16x32_f16 v[58:61], v[74:77], v[38:41], v[58:61]
	v_mfma_f32_16x16x32_f16 v[86:89], v[74:77], v[156:159], v[94:97]
	v_mfma_f32_16x16x32_f16 v[94:97], v[74:77], v[160:163], v[176:179]
	v_mfma_f32_16x16x32_f16 v[70:73], v[74:77], v[228:231], v[70:73]
	s_waitcnt vmcnt(18)
	v_mfma_f32_16x16x32_f16 v[54:57], v[66:69], v[38:41], v[54:57]
	v_mfma_f32_16x16x32_f16 v[74:77], v[66:69], v[156:159], v[90:93]
	v_mfma_f32_16x16x32_f16 v[90:93], v[66:69], v[160:163], v[180:183]
	v_mfma_f32_16x16x32_f16 v[62:65], v[66:69], v[228:231], v[62:65]
	s_waitcnt vmcnt(17)
	v_mfma_f32_16x16x32_f16 v[38:41], v[46:49], v[38:41], v[50:53]
	v_mfma_f32_16x16x32_f16 v[50:53], v[46:49], v[156:159], v[78:81]
	v_mfma_f32_16x16x32_f16 v[66:69], v[46:49], v[160:163], v[122:125]
	s_nop 1
	buffer_load_dwordx4 v[78:81], v147, s[16:19], s8 offen
	buffer_load_dwordx4 v[122:125], v148, s[16:19], s8 offen
	buffer_load_dwordx4 v[156:159], v149, s[16:19], s8 offen
	buffer_load_dwordx4 v[160:163], v150, s[16:19], s8 offen
	v_mfma_f32_16x16x32_f16 v[34:37], v[46:49], v[228:231], v[34:37]
	v_add_u32_e32 v98, s69, v98
	ds_read_b128 v[46:49], v98
	ds_read_b128 v[176:179], v98 offset:16384
	ds_read_b128 v[180:183], v98 offset:32768
	ds_read_b128 v[228:231], v98 offset:49152
	s_add_i32 s8, s22, s38
	s_waitcnt vmcnt(20) lgkmcnt(7)
	v_mfma_f32_16x16x32_f16 v[164:167], v[192:195], v[42:45], v[164:167]
	s_waitcnt lgkmcnt(6)
	v_mfma_f32_16x16x32_f16 v[168:171], v[192:195], v[208:211], v[168:171]
	s_waitcnt lgkmcnt(5)
	v_mfma_f32_16x16x32_f16 v[172:175], v[192:195], v[212:215], v[172:175]
	s_waitcnt lgkmcnt(4)
	v_mfma_f32_16x16x32_f16 v[82:85], v[192:195], v[216:219], v[82:85]
	s_waitcnt vmcnt(19)
	v_mfma_f32_16x16x32_f16 v[58:61], v[196:199], v[42:45], v[58:61]
	v_mfma_f32_16x16x32_f16 v[86:89], v[196:199], v[208:211], v[86:89]
	v_mfma_f32_16x16x32_f16 v[94:97], v[196:199], v[212:215], v[94:97]
	v_mfma_f32_16x16x32_f16 v[70:73], v[196:199], v[216:219], v[70:73]
	s_waitcnt vmcnt(18)
	v_mfma_f32_16x16x32_f16 v[54:57], v[200:203], v[42:45], v[54:57]
	v_mfma_f32_16x16x32_f16 v[74:77], v[200:203], v[208:211], v[74:77]
	v_mfma_f32_16x16x32_f16 v[90:93], v[200:203], v[212:215], v[90:93]
	v_mfma_f32_16x16x32_f16 v[62:65], v[200:203], v[216:219], v[62:65]
	s_waitcnt vmcnt(17)
	v_mfma_f32_16x16x32_f16 v[38:41], v[204:207], v[42:45], v[38:41]
	v_mfma_f32_16x16x32_f16 v[42:45], v[204:207], v[208:211], v[50:53]
	v_mfma_f32_16x16x32_f16 v[50:53], v[204:207], v[212:215], v[66:69]
	s_nop 2
	buffer_load_dwordx4 v[66:69], v147, s[16:19], s8 offen
	buffer_load_dwordx4 v[192:195], v148, s[16:19], s8 offen
	buffer_load_dwordx4 v[196:199], v149, s[16:19], s8 offen
	buffer_load_dwordx4 v[200:203], v150, s[16:19], s8 offen
	v_mfma_f32_16x16x32_f16 v[34:37], v[204:207], v[216:219], v[34:37]
	v_add_u32_e32 v99, s70, v99
	ds_read_b128 v[204:207], v99
	ds_read_b128 v[208:211], v99 offset:16384
	ds_read_b128 v[212:215], v99 offset:32768
	ds_read_b128 v[216:219], v99 offset:49152
	s_add_i32 s8, s22, s39
	s_waitcnt vmcnt(20) lgkmcnt(7)
	v_mfma_f32_16x16x32_f16 v[164:167], v[140:143], v[46:49], v[164:167]
	s_waitcnt lgkmcnt(6)
	v_mfma_f32_16x16x32_f16 v[168:171], v[140:143], v[176:179], v[168:171]
	s_waitcnt lgkmcnt(5)
	v_mfma_f32_16x16x32_f16 v[172:175], v[140:143], v[180:183], v[172:175]
	s_waitcnt lgkmcnt(4)
	v_mfma_f32_16x16x32_f16 v[82:85], v[140:143], v[228:231], v[82:85]
	s_waitcnt vmcnt(19)
	v_mfma_f32_16x16x32_f16 v[58:61], v[220:223], v[46:49], v[58:61]
	v_mfma_f32_16x16x32_f16 v[86:89], v[220:223], v[176:179], v[86:89]
	s_waitcnt vmcnt(18)
	v_mfma_f32_16x16x32_f16 v[54:57], v[152:155], v[46:49], v[54:57]
	v_mfma_f32_16x16x32_f16 v[74:77], v[152:155], v[176:179], v[74:77]
	v_mfma_f32_16x16x32_f16 v[90:93], v[152:155], v[180:183], v[90:93]
	v_mfma_f32_16x16x32_f16 v[62:65], v[152:155], v[228:231], v[62:65]
	s_waitcnt vmcnt(17)
	v_mfma_f32_16x16x32_f16 v[38:41], v[224:227], v[46:49], v[38:41]
	v_mfma_f32_16x16x32_f16 v[42:45], v[224:227], v[176:179], v[42:45]
	v_mfma_f32_16x16x32_f16 v[46:49], v[224:227], v[180:183], v[50:53]
	s_nop 2
	buffer_load_dwordx4 v[50:53], v147, s[16:19], s8 offen
	buffer_load_dwordx4 v[140:143], v148, s[16:19], s8 offen
	buffer_load_dwordx4 v[152:155], v149, s[16:19], s8 offen
	buffer_load_dwordx4 v[176:179], v150, s[16:19], s8 offen
	v_mfma_f32_16x16x32_f16 v[94:97], v[220:223], v[180:183], v[94:97]
	v_mfma_f32_16x16x32_f16 v[70:73], v[220:223], v[228:231], v[70:73]
	v_mfma_f32_16x16x32_f16 v[34:37], v[224:227], v[228:231], v[34:37]
	v_add_u32_e32 v100, s71, v100
	ds_read_b128 v[180:183], v100
	ds_read_b128 v[220:223], v100 offset:16384
	ds_read_b128 v[224:227], v100 offset:32768
	ds_read_b128 v[228:231], v100 offset:49152
	s_add_i32 s8, s22, s40
	s_waitcnt vmcnt(15) lgkmcnt(7)
	v_mfma_f32_16x16x32_f16 v[164:167], v[126:129], v[204:207], v[164:167]
	s_waitcnt lgkmcnt(6)
	v_mfma_f32_16x16x32_f16 v[168:171], v[126:129], v[208:211], v[168:171]
	s_waitcnt lgkmcnt(5)
	v_mfma_f32_16x16x32_f16 v[172:175], v[126:129], v[212:215], v[172:175]
	s_waitcnt lgkmcnt(4)
	v_mfma_f32_16x16x32_f16 v[82:85], v[126:129], v[216:219], v[82:85]
	s_waitcnt vmcnt(14)
	v_mfma_f32_16x16x32_f16 v[58:61], v[136:139], v[204:207], v[58:61]
	v_mfma_f32_16x16x32_f16 v[86:89], v[136:139], v[208:211], v[86:89]
	v_mfma_f32_16x16x32_f16 v[94:97], v[136:139], v[212:215], v[94:97]
	v_mfma_f32_16x16x32_f16 v[70:73], v[136:139], v[216:219], v[70:73]
	s_waitcnt vmcnt(13)
	v_mfma_f32_16x16x32_f16 v[54:57], v[184:187], v[204:207], v[54:57]
	v_mfma_f32_16x16x32_f16 v[74:77], v[184:187], v[208:211], v[74:77]
	v_mfma_f32_16x16x32_f16 v[90:93], v[184:187], v[212:215], v[90:93]
	v_mfma_f32_16x16x32_f16 v[62:65], v[184:187], v[216:219], v[62:65]
	s_waitcnt vmcnt(12)
	v_mfma_f32_16x16x32_f16 v[38:41], v[188:191], v[204:207], v[38:41]
	buffer_load_dwordx4 v[126:129], v147, s[16:19], s8 offen
	buffer_load_dwordx4 v[136:139], v148, s[16:19], s8 offen
	buffer_load_dwordx4 v[184:187], v149, s[16:19], s8 offen
	buffer_load_dwordx4 v[204:207], v150, s[16:19], s8 offen
	v_mfma_f32_16x16x32_f16 v[42:45], v[188:191], v[208:211], v[42:45]
	v_mfma_f32_16x16x32_f16 v[46:49], v[188:191], v[212:215], v[46:49]
	v_mfma_f32_16x16x32_f16 v[34:37], v[188:191], v[216:219], v[34:37]
	v_add_u32_e32 v111, s72, v111
	ds_read_b128 v[188:191], v111
	ds_read_b128 v[208:211], v111 offset:16384
	ds_read_b128 v[212:215], v111 offset:32768
	ds_read_b128 v[216:219], v111 offset:49152
	s_add_i32 s8, s22, s41
	s_waitcnt vmcnt(15) lgkmcnt(7)
	v_mfma_f32_16x16x32_f16 v[164:167], v[78:81], v[180:183], v[164:167]
	s_waitcnt lgkmcnt(6)
	v_mfma_f32_16x16x32_f16 v[168:171], v[78:81], v[220:223], v[168:171]
	s_waitcnt lgkmcnt(5)
	v_mfma_f32_16x16x32_f16 v[172:175], v[78:81], v[224:227], v[172:175]
	s_waitcnt lgkmcnt(4)
	v_mfma_f32_16x16x32_f16 v[78:81], v[78:81], v[228:231], v[82:85]
	s_waitcnt vmcnt(14)
	v_mfma_f32_16x16x32_f16 v[58:61], v[122:125], v[180:183], v[58:61]
	v_mfma_f32_16x16x32_f16 v[82:85], v[122:125], v[220:223], v[86:89]
	v_mfma_f32_16x16x32_f16 v[86:89], v[122:125], v[224:227], v[94:97]
	v_mfma_f32_16x16x32_f16 v[70:73], v[122:125], v[228:231], v[70:73]
	s_waitcnt vmcnt(13)
	v_mfma_f32_16x16x32_f16 v[54:57], v[156:159], v[180:183], v[54:57]
	v_mfma_f32_16x16x32_f16 v[74:77], v[156:159], v[220:223], v[74:77]
	v_mfma_f32_16x16x32_f16 v[90:93], v[156:159], v[224:227], v[90:93]
	v_mfma_f32_16x16x32_f16 v[62:65], v[156:159], v[228:231], v[62:65]
	s_waitcnt vmcnt(12)
	v_mfma_f32_16x16x32_f16 v[38:41], v[160:163], v[180:183], v[38:41]
	buffer_load_dwordx4 v[94:97], v147, s[16:19], s8 offen
	buffer_load_dwordx4 v[122:125], v148, s[16:19], s8 offen
	buffer_load_dwordx4 v[156:159], v149, s[16:19], s8 offen
	buffer_load_dwordx4 v[180:183], v150, s[16:19], s8 offen
	v_mfma_f32_16x16x32_f16 v[42:45], v[160:163], v[220:223], v[42:45]
	v_mfma_f32_16x16x32_f16 v[46:49], v[160:163], v[224:227], v[46:49]
	v_mfma_f32_16x16x32_f16 v[34:37], v[160:163], v[228:231], v[34:37]
	v_add_u32_e32 v98, s73, v98
	ds_read_b128 v[160:163], v98
	ds_read_b128 v[220:223], v98 offset:16384
	ds_read_b128 v[224:227], v98 offset:32768
	ds_read_b128 v[228:231], v98 offset:49152
	s_add_i32 s8, s22, s42
	s_waitcnt vmcnt(15) lgkmcnt(7)
	v_mfma_f32_16x16x32_f16 v[164:167], v[66:69], v[188:191], v[164:167]
	s_waitcnt lgkmcnt(6)
	v_mfma_f32_16x16x32_f16 v[168:171], v[66:69], v[208:211], v[168:171]
	s_waitcnt lgkmcnt(5)
	v_mfma_f32_16x16x32_f16 v[172:175], v[66:69], v[212:215], v[172:175]
	s_waitcnt lgkmcnt(4)
	v_mfma_f32_16x16x32_f16 v[66:69], v[66:69], v[216:219], v[78:81]
	s_waitcnt vmcnt(14)
	v_mfma_f32_16x16x32_f16 v[58:61], v[192:195], v[188:191], v[58:61]
	v_mfma_f32_16x16x32_f16 v[78:81], v[192:195], v[208:211], v[82:85]
	v_mfma_f32_16x16x32_f16 v[82:85], v[192:195], v[212:215], v[86:89]
	v_mfma_f32_16x16x32_f16 v[70:73], v[192:195], v[216:219], v[70:73]
	s_waitcnt vmcnt(13)
	v_mfma_f32_16x16x32_f16 v[54:57], v[196:199], v[188:191], v[54:57]
	v_mfma_f32_16x16x32_f16 v[74:77], v[196:199], v[208:211], v[74:77]
	v_mfma_f32_16x16x32_f16 v[86:89], v[196:199], v[212:215], v[90:93]
	v_mfma_f32_16x16x32_f16 v[62:65], v[196:199], v[216:219], v[62:65]
	s_waitcnt vmcnt(12)
	v_mfma_f32_16x16x32_f16 v[38:41], v[200:203], v[188:191], v[38:41]
	buffer_load_dwordx4 v[90:93], v147, s[16:19], s8 offen
	buffer_load_dwordx4 v[188:191], v148, s[16:19], s8 offen
	buffer_load_dwordx4 v[192:195], v149, s[16:19], s8 offen
	buffer_load_dwordx4 v[196:199], v150, s[16:19], s8 offen
	v_mfma_f32_16x16x32_f16 v[42:45], v[200:203], v[208:211], v[42:45]
	v_mfma_f32_16x16x32_f16 v[46:49], v[200:203], v[212:215], v[46:49]
	v_mfma_f32_16x16x32_f16 v[34:37], v[200:203], v[216:219], v[34:37]
	v_add_u32_e32 v99, s74, v99
	ds_read_b128 v[200:203], v99
	ds_read_b128 v[208:211], v99 offset:16384
	ds_read_b128 v[212:215], v99 offset:32768
	ds_read_b128 v[216:219], v99 offset:49152
	s_add_i32 s8, s22, s43
	s_waitcnt vmcnt(15) lgkmcnt(7)
	v_mfma_f32_16x16x32_f16 v[164:167], v[50:53], v[160:163], v[164:167]
	s_waitcnt lgkmcnt(6)
	v_mfma_f32_16x16x32_f16 v[168:171], v[50:53], v[220:223], v[168:171]
	s_waitcnt lgkmcnt(5)
	v_mfma_f32_16x16x32_f16 v[172:175], v[50:53], v[224:227], v[172:175]
	s_waitcnt lgkmcnt(4)
	v_mfma_f32_16x16x32_f16 v[50:53], v[50:53], v[228:231], v[66:69]
	s_waitcnt vmcnt(14)
	v_mfma_f32_16x16x32_f16 v[58:61], v[140:143], v[160:163], v[58:61]
	v_mfma_f32_16x16x32_f16 v[66:69], v[140:143], v[220:223], v[78:81]
	v_mfma_f32_16x16x32_f16 v[78:81], v[140:143], v[224:227], v[82:85]
	v_mfma_f32_16x16x32_f16 v[70:73], v[140:143], v[228:231], v[70:73]
	s_waitcnt vmcnt(13)
	v_mfma_f32_16x16x32_f16 v[54:57], v[152:155], v[160:163], v[54:57]
	v_mfma_f32_16x16x32_f16 v[74:77], v[152:155], v[220:223], v[74:77]
	v_mfma_f32_16x16x32_f16 v[82:85], v[152:155], v[224:227], v[86:89]
	v_mfma_f32_16x16x32_f16 v[62:65], v[152:155], v[228:231], v[62:65]
	s_waitcnt vmcnt(12)
	v_mfma_f32_16x16x32_f16 v[38:41], v[176:179], v[160:163], v[38:41]
	buffer_load_dwordx4 v[86:89], v147, s[16:19], s8 offen
	buffer_load_dwordx4 v[140:143], v148, s[16:19], s8 offen
	buffer_load_dwordx4 v[152:155], v149, s[16:19], s8 offen
	buffer_load_dwordx4 v[160:163], v150, s[16:19], s8 offen
	v_mfma_f32_16x16x32_f16 v[42:45], v[176:179], v[220:223], v[42:45]
	v_mfma_f32_16x16x32_f16 v[46:49], v[176:179], v[224:227], v[46:49]
	v_mfma_f32_16x16x32_f16 v[34:37], v[176:179], v[228:231], v[34:37]
	v_add_u32_e32 v100, s75, v100
	ds_read_b128 v[176:179], v100
	ds_read_b128 v[220:223], v100 offset:16384
	ds_read_b128 v[224:227], v100 offset:32768
	ds_read_b128 v[228:231], v100 offset:49152
	s_add_i32 s8, s22, s44
	s_waitcnt vmcnt(15) lgkmcnt(7)
	v_mfma_f32_16x16x32_f16 v[164:167], v[126:129], v[200:203], v[164:167]
	s_waitcnt lgkmcnt(6)
	v_mfma_f32_16x16x32_f16 v[168:171], v[126:129], v[208:211], v[168:171]
	s_waitcnt lgkmcnt(5)
	v_mfma_f32_16x16x32_f16 v[172:175], v[126:129], v[212:215], v[172:175]
	s_waitcnt lgkmcnt(4)
	v_mfma_f32_16x16x32_f16 v[50:53], v[126:129], v[216:219], v[50:53]
	s_waitcnt vmcnt(14)
	v_mfma_f32_16x16x32_f16 v[58:61], v[136:139], v[200:203], v[58:61]
	v_mfma_f32_16x16x32_f16 v[66:69], v[136:139], v[208:211], v[66:69]
	v_mfma_f32_16x16x32_f16 v[78:81], v[136:139], v[212:215], v[78:81]
	v_mfma_f32_16x16x32_f16 v[70:73], v[136:139], v[216:219], v[70:73]
	s_waitcnt vmcnt(13)
	v_mfma_f32_16x16x32_f16 v[54:57], v[184:187], v[200:203], v[54:57]
	v_mfma_f32_16x16x32_f16 v[74:77], v[184:187], v[208:211], v[74:77]
	v_mfma_f32_16x16x32_f16 v[82:85], v[184:187], v[212:215], v[82:85]
	v_mfma_f32_16x16x32_f16 v[62:65], v[184:187], v[216:219], v[62:65]
	s_waitcnt vmcnt(12)
	v_mfma_f32_16x16x32_f16 v[38:41], v[204:207], v[200:203], v[38:41]
	buffer_load_dwordx4 v[126:129], v147, s[16:19], s8 offen
	buffer_load_dwordx4 v[136:139], v148, s[16:19], s8 offen
	buffer_load_dwordx4 v[184:187], v149, s[16:19], s8 offen
	buffer_load_dwordx4 v[200:203], v150, s[16:19], s8 offen
	v_mfma_f32_16x16x32_f16 v[42:45], v[204:207], v[208:211], v[42:45]
	v_mfma_f32_16x16x32_f16 v[46:49], v[204:207], v[212:215], v[46:49]
	v_mfma_f32_16x16x32_f16 v[34:37], v[204:207], v[216:219], v[34:37]
	v_add_u32_e32 v111, s76, v111
	ds_read_b128 v[204:207], v111
	ds_read_b128 v[208:211], v111 offset:16384
	ds_read_b128 v[212:215], v111 offset:32768
	ds_read_b128 v[216:219], v111 offset:49152
	s_add_i32 s8, s22, s45
	s_waitcnt vmcnt(15) lgkmcnt(7)
	v_mfma_f32_16x16x32_f16 v[164:167], v[94:97], v[176:179], v[164:167]
	s_waitcnt lgkmcnt(6)
	v_mfma_f32_16x16x32_f16 v[168:171], v[94:97], v[220:223], v[168:171]
	s_waitcnt vmcnt(14)
	v_mfma_f32_16x16x32_f16 v[58:61], v[122:125], v[176:179], v[58:61]
	v_mfma_f32_16x16x32_f16 v[66:69], v[122:125], v[220:223], v[66:69]
	s_waitcnt lgkmcnt(5)
	v_mfma_f32_16x16x32_f16 v[78:81], v[122:125], v[224:227], v[78:81]
	s_waitcnt lgkmcnt(4)
	v_mfma_f32_16x16x32_f16 v[70:73], v[122:125], v[228:231], v[70:73]
	s_waitcnt vmcnt(13)
	v_mfma_f32_16x16x32_f16 v[54:57], v[156:159], v[176:179], v[54:57]
	v_mfma_f32_16x16x32_f16 v[74:77], v[156:159], v[220:223], v[74:77]
	v_mfma_f32_16x16x32_f16 v[82:85], v[156:159], v[224:227], v[82:85]
	v_mfma_f32_16x16x32_f16 v[62:65], v[156:159], v[228:231], v[62:65]
	s_waitcnt vmcnt(12)
	v_mfma_f32_16x16x32_f16 v[38:41], v[180:183], v[176:179], v[38:41]
	v_mfma_f32_16x16x32_f16 v[42:45], v[180:183], v[220:223], v[42:45]
	buffer_load_dwordx4 v[122:125], v147, s[16:19], s8 offen
	buffer_load_dwordx4 v[156:159], v148, s[16:19], s8 offen
	buffer_load_dwordx4 v[176:179], v149, s[16:19], s8 offen
	buffer_load_dwordx4 v[220:223], v150, s[16:19], s8 offen
	v_mfma_f32_16x16x32_f16 v[50:53], v[94:97], v[228:231], v[50:53]
	v_mfma_f32_16x16x32_f16 v[46:49], v[180:183], v[224:227], v[46:49]
	v_mfma_f32_16x16x32_f16 v[34:37], v[180:183], v[228:231], v[34:37]
	v_mfma_f32_16x16x32_f16 v[172:175], v[94:97], v[224:227], v[172:175]
	v_add_u32_e32 v98, s77, v98
	ds_read_b128 v[94:97], v98
	ds_read_b128 v[180:183], v98 offset:16384
	ds_read_b128 v[224:227], v98 offset:32768
	ds_read_b128 v[228:231], v98 offset:49152
	s_add_i32 s8, s22, s46
	s_waitcnt vmcnt(15) lgkmcnt(7)
	v_mfma_f32_16x16x32_f16 v[164:167], v[90:93], v[204:207], v[164:167]
	s_waitcnt lgkmcnt(6)
	v_mfma_f32_16x16x32_f16 v[168:171], v[90:93], v[208:211], v[168:171]
	s_waitcnt lgkmcnt(5)
	v_mfma_f32_16x16x32_f16 v[172:175], v[90:93], v[212:215], v[172:175]
	s_waitcnt lgkmcnt(4)
	v_mfma_f32_16x16x32_f16 v[90:93], v[90:93], v[216:219], v[50:53]
	s_waitcnt vmcnt(14)
	v_mfma_f32_16x16x32_f16 v[232:235], v[188:191], v[204:207], v[58:61]
	v_mfma_f32_16x16x32_f16 v[66:69], v[188:191], v[208:211], v[66:69]
	v_mfma_f32_16x16x32_f16 v[78:81], v[188:191], v[212:215], v[78:81]
	v_mfma_f32_16x16x32_f16 v[70:73], v[188:191], v[216:219], v[70:73]
	s_waitcnt vmcnt(13)
	v_mfma_f32_16x16x32_f16 v[188:191], v[192:195], v[204:207], v[54:57]
	v_mfma_f32_16x16x32_f16 v[74:77], v[192:195], v[208:211], v[74:77]
	v_mfma_f32_16x16x32_f16 v[82:85], v[192:195], v[212:215], v[82:85]
	v_mfma_f32_16x16x32_f16 v[62:65], v[192:195], v[216:219], v[62:65]
	s_waitcnt vmcnt(12)
	v_mfma_f32_16x16x32_f16 v[192:195], v[196:199], v[204:207], v[38:41]
	buffer_load_dwordx4 v[58:61], v147, s[16:19], s8 offen
	buffer_load_dwordx4 v[54:57], v148, s[16:19], s8 offen
	buffer_load_dwordx4 v[50:53], v149, s[16:19], s8 offen
	buffer_load_dwordx4 v[38:41], v150, s[16:19], s8 offen
	v_mfma_f32_16x16x32_f16 v[42:45], v[196:199], v[208:211], v[42:45]
	v_mfma_f32_16x16x32_f16 v[46:49], v[196:199], v[212:215], v[46:49]
	v_mfma_f32_16x16x32_f16 v[196:199], v[196:199], v[216:219], v[34:37]
	v_add_u32_e32 v99, s78, v99
	ds_read_b128 v[204:207], v99
	ds_read_b128 v[208:211], v99 offset:16384
	ds_read_b128 v[212:215], v99 offset:32768
	ds_read_b128 v[216:219], v99 offset:49152
	s_add_i32 s8, s22, s47
	s_waitcnt vmcnt(15) lgkmcnt(7)
	v_mfma_f32_16x16x32_f16 v[164:167], v[86:89], v[94:97], v[164:167]
	s_waitcnt lgkmcnt(6)
	v_mfma_f32_16x16x32_f16 v[168:171], v[86:89], v[180:183], v[168:171]
	s_waitcnt lgkmcnt(5)
	v_mfma_f32_16x16x32_f16 v[172:175], v[86:89], v[224:227], v[172:175]
	s_waitcnt lgkmcnt(4)
	v_mfma_f32_16x16x32_f16 v[86:89], v[86:89], v[228:231], v[90:93]
	s_waitcnt vmcnt(14)
	v_mfma_f32_16x16x32_f16 v[232:235], v[140:143], v[94:97], v[232:235]
	v_mfma_f32_16x16x32_f16 v[66:69], v[140:143], v[180:183], v[66:69]
	v_mfma_f32_16x16x32_f16 v[236:239], v[140:143], v[224:227], v[78:81]
	v_mfma_f32_16x16x32_f16 v[70:73], v[140:143], v[228:231], v[70:73]
	s_waitcnt vmcnt(13)
	v_mfma_f32_16x16x32_f16 v[140:143], v[152:155], v[94:97], v[188:191]
	v_mfma_f32_16x16x32_f16 v[74:77], v[152:155], v[180:183], v[74:77]
	v_mfma_f32_16x16x32_f16 v[82:85], v[152:155], v[224:227], v[82:85]
	v_mfma_f32_16x16x32_f16 v[62:65], v[152:155], v[228:231], v[62:65]
	s_waitcnt vmcnt(12)
	v_mfma_f32_16x16x32_f16 v[152:155], v[160:163], v[94:97], v[192:195]
	buffer_load_dwordx4 v[94:97], v147, s[16:19], s8 offen
	buffer_load_dwordx4 v[90:93], v148, s[16:19], s8 offen
	buffer_load_dwordx4 v[78:81], v149, s[16:19], s8 offen
	buffer_load_dwordx4 v[34:37], v150, s[16:19], s8 offen
	v_mfma_f32_16x16x32_f16 v[42:45], v[160:163], v[180:183], v[42:45]
	v_mfma_f32_16x16x32_f16 v[46:49], v[160:163], v[224:227], v[46:49]
	v_mfma_f32_16x16x32_f16 v[160:163], v[160:163], v[228:231], v[196:199]
	v_add_u32_e32 v100, s79, v100
	ds_read_b128 v[180:183], v100
	ds_read_b128 v[188:191], v100 offset:16384
	ds_read_b128 v[192:195], v100 offset:32768
	ds_read_b128 v[196:199], v100 offset:49152
	s_add_i32 s8, s22, s48
	s_waitcnt vmcnt(15) lgkmcnt(7)
	v_mfma_f32_16x16x32_f16 v[164:167], v[126:129], v[204:207], v[164:167]
	s_waitcnt lgkmcnt(6)
	v_mfma_f32_16x16x32_f16 v[168:171], v[126:129], v[208:211], v[168:171]
	s_waitcnt lgkmcnt(5)
	v_mfma_f32_16x16x32_f16 v[172:175], v[126:129], v[212:215], v[172:175]
	s_waitcnt lgkmcnt(4)
	v_mfma_f32_16x16x32_f16 v[86:89], v[126:129], v[216:219], v[86:89]
	s_waitcnt vmcnt(14)
	v_mfma_f32_16x16x32_f16 v[126:129], v[136:139], v[204:207], v[232:235]
	v_mfma_f32_16x16x32_f16 v[66:69], v[136:139], v[208:211], v[66:69]
	v_mfma_f32_16x16x32_f16 v[224:227], v[136:139], v[212:215], v[236:239]
	v_mfma_f32_16x16x32_f16 v[136:139], v[136:139], v[216:219], v[70:73]
	s_waitcnt vmcnt(13)
	v_mfma_f32_16x16x32_f16 v[140:143], v[184:187], v[204:207], v[140:143]
	v_mfma_f32_16x16x32_f16 v[74:77], v[184:187], v[208:211], v[74:77]
	v_mfma_f32_16x16x32_f16 v[228:231], v[184:187], v[212:215], v[82:85]
	v_mfma_f32_16x16x32_f16 v[184:187], v[184:187], v[216:219], v[62:65]
	s_waitcnt vmcnt(12)
	v_mfma_f32_16x16x32_f16 v[152:155], v[200:203], v[204:207], v[152:155]
	v_mfma_f32_16x16x32_f16 v[204:207], v[200:203], v[208:211], v[42:45]
	buffer_load_dwordx4 v[82:85], v147, s[16:19], s8 offen
	buffer_load_dwordx4 v[70:73], v148, s[16:19], s8 offen
	buffer_load_dwordx4 v[62:65], v149, s[16:19], s8 offen
	buffer_load_dwordx4 v[42:45], v150, s[16:19], s8 offen
	v_mfma_f32_16x16x32_f16 v[46:49], v[200:203], v[212:215], v[46:49]
	v_mfma_f32_16x16x32_f16 v[160:163], v[200:203], v[216:219], v[160:163]
	v_add_u32_e32 v0, 0x1ac00, v104
	ds_read_b128 v[240:243], v0
	ds_read_b128 v[244:247], v0 offset:16
	s_waitcnt vmcnt(12) lgkmcnt(5)
	v_mfma_f32_16x16x32_f16 v[164:167], v[122:125], v[180:183], v[164:167]
	v_mfma_f32_16x16x32_f16 v[126:129], v[156:159], v[180:183], v[126:129]
	v_mfma_f32_16x16x32_f16 v[140:143], v[176:179], v[180:183], v[140:143]
	v_mfma_f32_16x16x32_f16 v[152:155], v[220:223], v[180:183], v[152:155]
	s_waitcnt lgkmcnt(4)
	v_mfma_f32_16x16x32_f16 v[168:171], v[122:125], v[188:191], v[168:171]
	v_mfma_f32_16x16x32_f16 v[208:211], v[156:159], v[188:191], v[66:69]
	v_mfma_f32_16x16x32_f16 v[212:215], v[176:179], v[188:191], v[74:77]
	v_mfma_f32_16x16x32_f16 v[204:207], v[220:223], v[188:191], v[204:207]
	s_waitcnt lgkmcnt(3)
	v_mfma_f32_16x16x32_f16 v[172:175], v[122:125], v[192:195], v[172:175]
	v_cvt_pk_f16_f32 v232, v164, v165
	v_cvt_pk_f16_f32 v233, v166, v167
	v_pk_max_f16 v232, v232, 0
	v_pk_max_f16 v233, v233, 0
	v_mfma_f32_16x16x32_f16 v[224:227], v[156:159], v[192:195], v[224:227]
	v_cvt_pk_f16_f32 v234, v126, v127
	v_cvt_pk_f16_f32 v235, v128, v129
	v_pk_max_f16 v234, v234, 0
	v_pk_max_f16 v235, v235, 0
	v_mfma_f32_16x16x32_f16 v[228:231], v[176:179], v[192:195], v[228:231]
	v_cvt_pk_f16_f32 v236, v140, v141
	v_cvt_pk_f16_f32 v237, v142, v143
	v_pk_max_f16 v236, v236, 0
	v_pk_max_f16 v237, v237, 0
	v_mfma_f32_16x16x32_f16 v[216:219], v[220:223], v[192:195], v[46:49]
	v_cvt_pk_f16_f32 v238, v152, v153
	v_cvt_pk_f16_f32 v239, v154, v155
	v_pk_max_f16 v238, v238, 0
	v_pk_max_f16 v239, v239, 0
	s_waitcnt lgkmcnt(2)
	v_mfma_f32_16x16x32_f16 v[200:203], v[122:125], v[196:199], v[86:89]
	v_cvt_pk_f16_f32 v180, v168, v169
	v_cvt_pk_f16_f32 v181, v170, v171
	v_pk_max_f16 v180, v180, 0
	v_pk_max_f16 v181, v181, 0
	s_add_i32 s8, s22, s49
	buffer_load_dwordx4 v[86:89], v147, s[16:19], s8 offen
	buffer_load_dwordx4 v[74:77], v148, s[16:19], s8 offen
	buffer_load_dwordx4 v[66:69], v149, s[16:19], s8 offen
	buffer_load_dwordx4 v[46:49], v150, s[16:19], s8 offen
	v_mfma_f32_16x16x32_f16 v[136:139], v[156:159], v[196:199], v[136:139]
	v_cvt_pk_f16_f32 v182, v208, v209
	v_cvt_pk_f16_f32 v183, v210, v211
	v_pk_max_f16 v182, v182, 0
	v_pk_max_f16 v183, v183, 0
	s_waitcnt lgkmcnt(1)
	v_mfma_f32_16x16x32_f16 v[252:255], v[240:243], v[232:235], 0
	v_cvt_pk_f16_f32 v232, v172, v173
	v_cvt_pk_f16_f32 v233, v174, v175
	v_pk_max_f16 v232, v232, 0
	v_pk_max_f16 v233, v233, 0
	v_mfma_f32_16x16x32_f16 v[184:187], v[176:179], v[196:199], v[184:187]
	v_cvt_pk_f16_f32 v188, v212, v213
	v_cvt_pk_f16_f32 v189, v214, v215
	v_pk_max_f16 v188, v188, 0
	v_pk_max_f16 v189, v189, 0
	s_waitcnt lgkmcnt(0)
	v_mfma_f32_16x16x32_f16 v[252:255], v[244:247], v[236:239], v[252:255]
	v_cvt_pk_f16_f32 v234, v224, v225
	v_cvt_pk_f16_f32 v235, v226, v227
	v_pk_max_f16 v234, v234, 0
	v_pk_max_f16 v235, v235, 0
	v_mfma_f32_16x16x32_f16 v[160:163], v[220:223], v[196:199], v[160:163]
	v_cvt_pk_f16_f32 v190, v204, v205
	v_cvt_pk_f16_f32 v191, v206, v207
	v_pk_max_f16 v190, v190, 0
	v_pk_max_f16 v191, v191, 0
	v_mfma_f32_16x16x32_f16 v[192:195], v[240:243], v[180:183], 0
	v_cvt_pk_f16_f32 v236, v228, v229
	v_cvt_pk_f16_f32 v237, v230, v231
	v_pk_max_f16 v236, v236, 0
	v_pk_max_f16 v237, v237, 0
	v_mfma_f32_16x16x32_f16 v[192:195], v[244:247], v[188:191], v[192:195]
	v_cvt_pk_f16_f32 v238, v216, v217
	v_cvt_pk_f16_f32 v239, v218, v219
	v_pk_max_f16 v238, v238, 0
	v_pk_max_f16 v239, v239, 0
	v_cvt_pk_f16_f32 v180, v200, v201
	v_cvt_pk_f16_f32 v181, v202, v203
	v_pk_max_f16 v180, v180, 0
	v_pk_max_f16 v181, v181, 0
	v_mfma_f32_16x16x32_f16 v[196:199], v[240:243], v[232:235], 0
	v_cvt_pk_f16_f32 v182, v136, v137
	v_cvt_pk_f16_f32 v183, v138, v139
	v_pk_max_f16 v182, v182, 0
	v_pk_max_f16 v183, v183, 0
	v_mfma_f32_16x16x32_f16 v[196:199], v[244:247], v[236:239], v[196:199]
	v_cvt_pk_f16_f32 v188, v184, v185
	v_cvt_pk_f16_f32 v189, v186, v187
	v_pk_max_f16 v188, v188, 0
	v_pk_max_f16 v189, v189, 0
	v_cvt_pk_f16_f32 v190, v160, v161
	v_cvt_pk_f16_f32 v191, v162, v163
	v_pk_max_f16 v190, v190, 0
	v_pk_max_f16 v191, v191, 0
	v_mfma_f32_16x16x32_f16 v[122:125], v[240:243], v[180:183], 0
	s_nop 0
	v_mfma_f32_16x16x32_f16 v[122:125], v[244:247], v[188:191], v[122:125]
	v_add_u32_e32 v145, 0x12c00, v105
	ds_read_b128 v[240:243], v145 offset:2048
	ds_read_b128 v[244:247], v145 offset:2064
	ds_read_b128 v[248:251], v145 offset:2080
	s_load_dword s30, s[12:13], 0x0
	v_cndmask_b32_e64 v0, v252, v192, s[2:3]
	ds_read_b128 v[252:255], v145 offset:2096
	ds_read_u16 v102, v114
	ds_read_u16 v103, v114 offset:512
	ds_read_u16 v115, v114 offset:1024
	ds_read_u16 v116, v114 offset:1536
	v_cndmask_b32_e64 v0, v0, v196, s[0:1]
	s_waitcnt vmcnt(16)
	v_cndmask_b32_e64 v1, v30, v134, s[0:1]
	v_bfi_b32 v30, s10, v1, v30
	v_perm_b32 v1, v22, v134, s24
	v_cndmask_b32_e64 v22, v22, v1, s[0:1]
	v_bfi_b32 v1, s10, v135, v18
	v_perm_b32 v121, v10, v135, s24
	v_cndmask_b32_e64 v18, v18, v1, s[0:1]
	v_cndmask_b32_e64 v10, v10, v121, s[0:1]
	v_cndmask_b32_e64 v0, v0, v122, s[26:27]
	ds_write_b32 v112, v0
	s_add_i32 s22, s22, 0x80000
	s_add_i32 s11, s11, 1
	s_add_u32 s12, s12, 4
	s_addc_u32 s13, s13, 0
	v_add_u32_e32 v104, 0x400, v104
	v_add_u32_e32 v105, 0x800, v105
	v_add_u32_e32 v114, 2, v114
	s_cmp_eq_u32 s22, 0x898000
	s_waitcnt lgkmcnt(0)
	s_barrier
	ds_read_b128 v[232:235], v113
	ds_read_b128 v[236:239], v113 offset:1024
	s_waitcnt lgkmcnt(0)
	v_add_f32_e32 v0, v232, v233
	v_add_f32_e32 v1, v234, v235
	v_add_f32_e32 v121, v236, v237
	v_add_f32_e32 v144, v238, v239
	v_add_f32_e32 v0, v0, v1
	v_add_f32_e32 v121, v121, v144
	v_add_f32_e32 v0, v0, v121
	v_add_f32_e32 v0, s30, v0
	ds_write_b32 v106, v0
	v_cvt_f16_f32_e32 v1, v0
	v_cvt_f16_f32_e32 v121, v0
	s_nop 1
	v_permlane16_swap_b32_e32 v1, v121
	v_mov_b32_e32 v144, v1
	v_mov_b32_e32 v145, v121
	s_nop 1
	v_permlane32_swap_b32_e32 v1, v144
	v_permlane32_swap_b32_e32 v121, v145
	v_add_u32_e32 v106, 4, v106
	s_cbranch_scc0 .LBB1_4

amdhsa.kernels:
  - .agpr_count:     0
    .args:
      - .actual_access:  read_only
        .address_space:  global
        .offset:         0
        .size:           8
        .value_kind:     global_buffer
      - .actual_access:  write_only
        .address_space:  global
        .offset:         8
        .size:           8
        .value_kind:     global_buffer
      - .actual_access:  read_only
        .address_space:  global
        .offset:         16
        .size:           8
        .value_kind:     global_buffer
      - .actual_access:  read_only
        .address_space:  global
        .offset:         24
        .size:           8
        .value_kind:     global_buffer
      - .actual_access:  read_only
        .address_space:  global
        .offset:         32
        .size:           8
        .value_kind:     global_buffer
      - .actual_access:  read_only
        .address_space:  global
        .offset:         40
        .size:           8
        .value_kind:     global_buffer
      - .actual_access:  read_only
        .address_space:  global
        .offset:         48
        .size:           8
        .value_kind:     global_buffer
      - .actual_access:  read_only
        .address_space:  global
        .offset:         56
        .size:           8
        .value_kind:     global_buffer
      - .actual_access:  read_only
        .address_space:  global
        .offset:         64
        .size:           8
        .value_kind:     global_buffer
      - .actual_access:  read_only
        .address_space:  global
        .offset:         72
        .size:           8
        .value_kind:     global_buffer
      - .actual_access:  read_only
        .address_space:  global
        .offset:         80
        .size:           8
        .value_kind:     global_buffer
      - .actual_access:  write_only
        .address_space:  global
        .offset:         88
        .size:           8
        .value_kind:     global_buffer
      - .actual_access:  write_only
        .address_space:  global
        .offset:         96
        .size:           8
        .value_kind:     global_buffer
      - .actual_access:  write_only
        .address_space:  global
        .offset:         104
        .size:           8
        .value_kind:     global_buffer
      - .actual_access:  write_only
        .address_space:  global
        .offset:         112
        .size:           8
        .value_kind:     global_buffer
      - .actual_access:  write_only
        .address_space:  global
        .offset:         120
        .size:           8
        .value_kind:     global_buffer
    .group_segment_fixed_size: 17440
    .kernarg_segment_align: 8
    .kernarg_segment_size: 128
    .language:       OpenCL C
    .language_version:
      - 2
      - 0
    .max_flat_workgroup_size: 256
    .name:           _Z11prep_kernelPKfPDv8_DF16_S0_S0_S0_S0_S0_S0_S0_S0_S0_S2_PfPDF16_S4_S3_
    .private_segment_fixed_size: 0
    .sgpr_count:     32
    .sgpr_spill_count: 0
    .symbol:         _Z11prep_kernelPKfPDv8_DF16_S0_S0_S0_S0_S0_S0_S0_S0_S0_S2_PfPDF16_S4_S3_.kd
    .uniform_work_group_size: 1
    .uses_dynamic_stack: false
    .vgpr_count:     42
    .vgpr_spill_count: 0
    .wavefront_size: 64
  - .agpr_count:     0
    .args:
      - .actual_access:  read_only
        .address_space:  global
        .offset:         0
        .size:           8
        .value_kind:     global_buffer
      - .actual_access:  read_only
        .address_space:  global
        .offset:         8
        .size:           8
        .value_kind:     global_buffer
      - .actual_access:  read_only
        .address_space:  global
        .offset:         16
        .size:           8
        .value_kind:     global_buffer
      - .actual_access:  read_only
        .address_space:  global
        .offset:         24
        .size:           8
        .value_kind:     global_buffer
      - .actual_access:  read_only
        .address_space:  global
        .offset:         32
        .size:           8
        .value_kind:     global_buffer
      - .actual_access:  read_only
        .address_space:  global
        .offset:         40
        .size:           8
        .value_kind:     global_buffer
      - .actual_access:  read_only
        .address_space:  global
        .offset:         48
        .size:           8
        .value_kind:     global_buffer
      - .actual_access:  read_only
        .address_space:  global
        .offset:         56
        .size:           8
        .value_kind:     global_buffer
      - .actual_access:  read_only
        .address_space:  global
        .offset:         64
        .size:           8
        .value_kind:     global_buffer
      - .actual_access:  write_only
        .address_space:  global
        .offset:         72
        .size:           8
        .value_kind:     global_buffer
    .group_segment_fixed_size: 130304
    .kernarg_segment_align: 8
    .kernarg_segment_size: 80
    .language:       OpenCL C
    .language_version:
      - 2
      - 0
    .max_flat_workgroup_size: 512
    .name:           _Z16pdag_main_kernelPKfS0_S0_PKDv8_DF16_S3_S0_PKDF16_S5_S0_Pf
    .private_segment_fixed_size: 0
    .sgpr_count:     92
    .sgpr_spill_count: 0
    .symbol:         _Z16pdag_main_kernelPKfS0_S0_PKDv8_DF16_S3_S0_PKDF16_S5_S0_Pf.kd
    .uniform_work_group_size: 1
    .uses_dynamic_stack: false
    .vgpr_count:     256
    .vgpr_spill_count: 0
    .wavefront_size: 64
